# speedup vs baseline: 1.0380x; 1.0045x over previous
_Z10head_fusedPKDF16_S0_S0_PKfS2_S2_S2_S2_S2_S2_S2_Pf:
	s_mulk_i32 s3, 0x1c8
	s_add_i32 s3, s3, s2
	s_and_b32 s2, s2, 7
	s_mulk_i32 s2, 0x39
	s_ashr_i32 s37, s3, 3
	s_and_b32 s3, s37, 1
	s_mulk_i32 s3, 0x1c8
	s_lshr_b32 s37, s37, 1
	s_add_i32 s37, s37, s2
	s_add_i32 s37, s37, s3
	s_load_dwordx8 s[20:27], s[0:1], 0x40
	s_load_dwordx4 s[28:31], s[0:1], 0x0
	s_load_dwordx2 s[10:11], s[0:1], 0x10
	s_load_dwordx8 s[12:19], s[0:1], 0x20
	s_mul_hi_i32 s2, s37, 0x8fb823ef
	s_add_i32 s2, s2, s37
	s_lshr_b32 s3, s2, 31
	s_ashr_i32 s35, s2, 8
	s_add_i32 s35, s35, s3
	s_mul_i32 s2, s35, 0xfffffe38
	s_add_i32 s40, s2, s37
	s_mov_b32 s2, 41
	s_mov_b32 s34, 0
	s_cmpk_lt_i32 s40, 0x148
	s_mov_b32 s3, 0
	s_cbranch_scc1 .LBB2_6
	s_cmpk_lt_u32 s40, 0x1a0
	s_cbranch_scc1 .LBB2_4
	s_cmpk_lt_u32 s40, 0x1b8
	s_cbranch_scc1 .LBB2_5
	s_cmpk_lt_u32 s40, 0x1c0
	s_movk_i32 s2, 0xfe48
	s_cselect_b32 s3, s2, 0xfffffe40
	s_cselect_b32 s34, 3, 4
	s_mov_b32 s2, 1
	s_branch .LBB2_6
